# last layer-2 MFMA pair split: first MFMA of the final partial issued before the last two relu/convert groups so its latency overlaps them
# speedup vs baseline: 1.0053x; 1.0053x over previous
.LBB1_4:
	s_and_saveexec_b64 s[8:9], s[2:3]
	v_perm_b32 v5, v1, v102, s23
	v_perm_b32 v9, v121, v103, s23
	s_or_b64 exec, exec, s[8:9]
	v_mov_b32_e32 v144, v1
	v_mov_b32_e32 v145, v121
	v_mfma_f32_16x16x32_f16 v[164:167], v[30:33], v[2:5], 0
	v_mfma_f32_16x16x32_f16 v[180:183], v[22:25], v[2:5], 0
	s_cmp_lg_u32 s22, 0x818000
	v_permlane32_swap_b32_e32 v1, v144
	v_permlane32_swap_b32_e32 v121, v145
	v_mfma_f32_16x16x32_f16 v[168:171], v[30:33], v[6:9], 0
	v_mfma_f32_16x16x32_f16 v[184:187], v[22:25], v[6:9], 0
	s_cselect_b32 s9, s11, 15
	s_and_saveexec_b64 s[32:33], s[2:3]
	v_perm_b32 v17, v144, v115, s23
	v_perm_b32 v29, v145, v116, s23
	s_or_b64 exec, exec, s[32:33]
	v_mfma_f32_16x16x32_f16 v[172:175], v[30:33], v[14:17], 0
	v_mfma_f32_16x16x32_f16 v[188:191], v[22:25], v[14:17], 0
	v_mfma_f32_16x16x32_f16 v[176:179], v[30:33], v[26:29], 0
	v_mfma_f32_16x16x32_f16 v[192:195], v[22:25], v[26:29], 0
	v_mfma_f32_16x16x32_f16 v[208:211], v[18:21], v[2:5], 0
	v_mfma_f32_16x16x32_f16 v[224:227], v[10:13], v[2:5], 0
	v_cvt_pk_f16_f32 v122, v164, v165
	v_cvt_pk_f16_f32 v123, v166, v167
	v_pk_max_f16 v122, v122, 0
	v_pk_max_f16 v123, v123, 0
	v_cvt_pk_f16_f32 v124, v180, v181
	v_cvt_pk_f16_f32 v125, v182, v183
	v_pk_max_f16 v124, v124, 0
	v_pk_max_f16 v125, v125, 0
	ds_write_b128 v107, v[122:125]
	v_mfma_f32_16x16x32_f16 v[212:215], v[18:21], v[6:9], 0
	v_mfma_f32_16x16x32_f16 v[228:231], v[10:13], v[6:9], 0
	v_cvt_pk_f16_f32 v126, v168, v169
	v_cvt_pk_f16_f32 v127, v170, v171
	v_pk_max_f16 v126, v126, 0
	v_pk_max_f16 v127, v127, 0
	v_cvt_pk_f16_f32 v128, v184, v185
	v_cvt_pk_f16_f32 v129, v186, v187
	v_pk_max_f16 v128, v128, 0
	v_pk_max_f16 v129, v129, 0
	ds_write_b128 v107, v[126:129] offset:16384
	v_mfma_f32_16x16x32_f16 v[216:219], v[18:21], v[14:17], 0
	v_mfma_f32_16x16x32_f16 v[232:235], v[10:13], v[14:17], 0
	v_cvt_pk_f16_f32 v134, v172, v173
	v_cvt_pk_f16_f32 v135, v174, v175
	v_pk_max_f16 v134, v134, 0
	v_pk_max_f16 v135, v135, 0
	v_cvt_pk_f16_f32 v136, v188, v189
	v_cvt_pk_f16_f32 v137, v190, v191
	v_pk_max_f16 v136, v136, 0
	v_pk_max_f16 v137, v137, 0
	ds_write_b128 v107, v[134:137] offset:32768
	v_mfma_f32_16x16x32_f16 v[220:223], v[18:21], v[26:29], 0
	v_mfma_f32_16x16x32_f16 v[236:239], v[10:13], v[26:29], 0
	v_cvt_pk_f16_f32 v138, v176, v177
	v_cvt_pk_f16_f32 v139, v178, v179
	v_pk_max_f16 v138, v138, 0
	v_pk_max_f16 v139, v139, 0
	v_cvt_pk_f16_f32 v140, v192, v193
	v_cvt_pk_f16_f32 v141, v194, v195
	v_pk_max_f16 v140, v140, 0
	v_pk_max_f16 v141, v141, 0
	ds_write_b128 v107, v[138:141] offset:49152
	v_add_u32_e32 v111, s64, v111
	v_add_u32_e32 v98, s65, v98
	s_lshl_b32 s20, s9, 7
	v_lshl_add_u64 v[0:1], s[20:21], 3, v[132:133]
	s_add_i32 s25, s22, s34
	s_lshl_b32 s8, s9, 8
	buffer_load_dwordx4 v[192:195], v147, s[16:19], s25 offen
	buffer_load_dwordx4 v[196:199], v148, s[16:19], s25 offen
	buffer_load_dwordx4 v[200:203], v149, s[16:19], s25 offen
	buffer_load_dwordx4 v[204:207], v150, s[16:19], s25 offen
	s_waitcnt vmcnt(19) lgkmcnt(4)
	v_mfma_f32_16x16x32_f16 v[164:167], v[58:61], v[122:125], v[240:243]
	s_load_dword s30, s[12:13], 0x0
	v_cvt_pk_f16_f32 v142, v208, v209
	v_cvt_pk_f16_f32 v143, v210, v211
	v_mfma_f32_16x16x32_f16 v[168:171], v[58:61], v[126:129], v[240:243]
	v_pk_max_f16 v142, v142, 0
	v_pk_max_f16 v143, v143, 0
	v_mfma_f32_16x16x32_f16 v[172:175], v[58:61], v[134:137], v[240:243]
	v_cvt_pk_f16_f32 v144, v224, v225
	v_cvt_pk_f16_f32 v145, v226, v227
	v_mfma_f32_16x16x32_f16 v[10:13], v[58:61], v[138:141], v[240:243]
	v_pk_max_f16 v144, v144, 0
	v_pk_max_f16 v145, v145, 0
	ds_write_b128 v108, v[142:145]
	s_waitcnt vmcnt(18)
	v_mfma_f32_16x16x32_f16 v[58:61], v[54:57], v[122:125], v[244:247]
	v_cvt_pk_f16_f32 v152, v212, v213
	v_cvt_pk_f16_f32 v153, v214, v215
	v_mfma_f32_16x16x32_f16 v[176:179], v[54:57], v[126:129], v[244:247]
	v_pk_max_f16 v152, v152, 0
	v_pk_max_f16 v153, v153, 0
	v_mfma_f32_16x16x32_f16 v[180:183], v[54:57], v[134:137], v[244:247]
	v_cvt_pk_f16_f32 v154, v228, v229
	v_cvt_pk_f16_f32 v155, v230, v231
	v_mfma_f32_16x16x32_f16 v[18:21], v[54:57], v[138:141], v[244:247]
	v_pk_max_f16 v154, v154, 0
	v_pk_max_f16 v155, v155, 0
	ds_write_b128 v108, v[152:155] offset:16384
	s_waitcnt vmcnt(17)
	v_mfma_f32_16x16x32_f16 v[54:57], v[50:53], v[122:125], v[248:251]
	v_cvt_pk_f16_f32 v156, v216, v217
	v_cvt_pk_f16_f32 v157, v218, v219
	v_mfma_f32_16x16x32_f16 v[184:187], v[50:53], v[126:129], v[248:251]
	v_pk_max_f16 v156, v156, 0
	v_pk_max_f16 v157, v157, 0
	v_mfma_f32_16x16x32_f16 v[188:191], v[50:53], v[134:137], v[248:251]
	v_cvt_pk_f16_f32 v158, v232, v233
	v_cvt_pk_f16_f32 v159, v234, v235
	v_mfma_f32_16x16x32_f16 v[22:25], v[50:53], v[138:141], v[248:251]
	v_pk_max_f16 v158, v158, 0
	v_pk_max_f16 v159, v159, 0
	ds_write_b128 v108, v[156:159] offset:32768
	s_waitcnt vmcnt(16)
	v_mfma_f32_16x16x32_f16 v[50:53], v[38:41], v[122:125], v[252:255]
	v_cvt_pk_f16_f32 v160, v220, v221
	v_cvt_pk_f16_f32 v161, v222, v223
	v_mfma_f32_16x16x32_f16 v[122:125], v[38:41], v[126:129], v[252:255]
	v_pk_max_f16 v160, v160, 0
	v_pk_max_f16 v161, v161, 0
	v_mfma_f32_16x16x32_f16 v[126:129], v[38:41], v[134:137], v[252:255]
	v_cvt_pk_f16_f32 v162, v236, v237
	v_cvt_pk_f16_f32 v163, v238, v239
	v_mfma_f32_16x16x32_f16 v[38:41], v[38:41], v[138:141], v[252:255]
	v_pk_max_f16 v162, v162, 0
	v_pk_max_f16 v163, v163, 0
	ds_write_b128 v108, v[160:163] offset:49152
	s_add_i32 s9, s22, s35
	s_waitcnt vmcnt(15)
	v_mfma_f32_16x16x32_f16 v[164:167], v[94:97], v[142:145], v[164:167]
	v_mfma_f32_16x16x32_f16 v[168:171], v[94:97], v[152:155], v[168:171]
	s_waitcnt vmcnt(14)
	v_mfma_f32_16x16x32_f16 v[58:61], v[90:93], v[142:145], v[58:61]
	v_mfma_f32_16x16x32_f16 v[176:179], v[90:93], v[152:155], v[176:179]
	s_waitcnt vmcnt(13)
	v_mfma_f32_16x16x32_f16 v[54:57], v[78:81], v[142:145], v[54:57]
	v_mfma_f32_16x16x32_f16 v[184:187], v[78:81], v[152:155], v[184:187]
	s_waitcnt vmcnt(12)
	v_mfma_f32_16x16x32_f16 v[50:53], v[34:37], v[142:145], v[50:53]
	buffer_load_dwordx4 v[140:143], v147, s[16:19], s9 offen
	buffer_load_dwordx4 v[220:223], v148, s[16:19], s9 offen
	v_mfma_f32_16x16x32_f16 v[122:125], v[34:37], v[152:155], v[122:125]
	buffer_load_dwordx4 v[152:155], v149, s[16:19], s9 offen
	buffer_load_dwordx4 v[224:227], v150, s[16:19], s9 offen
	s_mov_b32 s9, s21
	s_waitcnt lgkmcnt(0)
	s_barrier
	v_add_u32_e32 v99, s66, v99
	ds_read_b128 v[136:139], v99
	ds_read_b128 v[208:211], v99 offset:16384
	ds_read_b128 v[212:215], v99 offset:32768
	ds_read_b128 v[216:219], v99 offset:49152
	v_mfma_f32_16x16x32_f16 v[172:175], v[94:97], v[156:159], v[172:175]
	v_mfma_f32_16x16x32_f16 v[94:97], v[94:97], v[160:163], v[10:13]
	s_nop 2
	v_lshl_add_u64 v[10:11], s[8:9], 4, v[130:131]
	v_mfma_f32_16x16x32_f16 v[180:183], v[90:93], v[156:159], v[180:183]
	v_mfma_f32_16x16x32_f16 v[90:93], v[90:93], v[160:163], v[18:21]
	v_mfma_f32_16x16x32_f16 v[188:191], v[78:81], v[156:159], v[188:191]
	v_mfma_f32_16x16x32_f16 v[78:81], v[78:81], v[160:163], v[22:25]
	global_load_dwordx4 v[30:33], v[10:11], off
	s_nop 1
	global_load_dwordx4 v[22:25], v[10:11], off offset:1024
	global_load_dwordx4 v[18:21], v[10:11], off offset:2048
	s_nop 0
	global_load_dwordx4 v[10:13], v[10:11], off offset:3072
	s_nop 0
	global_load_dwordx2 v[134:135], v[0:1], off
	v_mfma_f32_16x16x32_f16 v[126:129], v[34:37], v[156:159], v[126:129]
	v_mfma_f32_16x16x32_f16 v[34:37], v[34:37], v[160:163], v[38:41]
	s_nop 2
	v_add_u32_e32 v100, s67, v100
	ds_read_b128 v[38:41], v100
	ds_read_b128 v[156:159], v100 offset:16384
	ds_read_b128 v[160:163], v100 offset:32768
	ds_read_b128 v[228:231], v100 offset:49152
	s_add_i32 s8, s22, s36
	s_waitcnt vmcnt(20) lgkmcnt(7)
	v_mfma_f32_16x16x32_f16 v[164:167], v[82:85], v[136:139], v[164:167]
	s_waitcnt lgkmcnt(6)
	v_mfma_f32_16x16x32_f16 v[168:171], v[82:85], v[208:211], v[168:171]
	s_waitcnt lgkmcnt(5)
	v_mfma_f32_16x16x32_f16 v[172:175], v[82:85], v[212:215], v[172:175]
	s_waitcnt lgkmcnt(4)
	v_mfma_f32_16x16x32_f16 v[82:85], v[82:85], v[216:219], v[94:97]
	s_waitcnt vmcnt(19)
	v_mfma_f32_16x16x32_f16 v[58:61], v[70:73], v[136:139], v[58:61]
	v_mfma_f32_16x16x32_f16 v[94:97], v[70:73], v[208:211], v[176:179]
	v_mfma_f32_16x16x32_f16 v[176:179], v[70:73], v[212:215], v[180:183]
	v_mfma_f32_16x16x32_f16 v[70:73], v[70:73], v[216:219], v[90:93]
	s_waitcnt vmcnt(18)
	v_mfma_f32_16x16x32_f16 v[54:57], v[62:65], v[136:139], v[54:57]
	v_mfma_f32_16x16x32_f16 v[90:93], v[62:65], v[208:211], v[184:187]
	v_mfma_f32_16x16x32_f16 v[180:183], v[62:65], v[212:215], v[188:191]
	v_mfma_f32_16x16x32_f16 v[62:65], v[62:65], v[216:219], v[78:81]
	s_waitcnt vmcnt(17)
	v_mfma_f32_16x16x32_f16 v[50:53], v[42:45], v[136:139], v[50:53]
	v_mfma_f32_16x16x32_f16 v[78:81], v[42:45], v[208:211], v[122:125]
	v_mfma_f32_16x16x32_f16 v[122:125], v[42:45], v[212:215], v[126:129]
	s_nop 2
	buffer_load_dwordx4 v[126:129], v147, s[16:19], s8 offen
	buffer_load_dwordx4 v[136:139], v148, s[16:19], s8 offen
	buffer_load_dwordx4 v[184:187], v149, s[16:19], s8 offen
	buffer_load_dwordx4 v[188:191], v150, s[16:19], s8 offen
	v_mfma_f32_16x16x32_f16 v[34:37], v[42:45], v[216:219], v[34:37]
	v_add_u32_e32 v111, s68, v111
	ds_read_b128 v[42:45], v111
	ds_read_b128 v[208:211], v111 offset:16384
	ds_read_b128 v[212:215], v111 offset:32768
	ds_read_b128 v[216:219], v111 offset:49152
	s_add_i32 s8, s22, s37
	s_waitcnt vmcnt(20) lgkmcnt(7)
	v_mfma_f32_16x16x32_f16 v[164:167], v[86:89], v[38:41], v[164:167]
	s_waitcnt lgkmcnt(6)
	v_mfma_f32_16x16x32_f16 v[168:171], v[86:89], v[156:159], v[168:171]
	s_waitcnt lgkmcnt(5)
	v_mfma_f32_16x16x32_f16 v[172:175], v[86:89], v[160:163], v[172:175]
	s_waitcnt lgkmcnt(4)
	v_mfma_f32_16x16x32_f16 v[82:85], v[86:89], v[228:231], v[82:85]
	s_waitcnt vmcnt(19)
	v_mfma_f32_16x16x32_f16 v[58:61], v[74:77], v[38:41], v[58:61]
	v_mfma_f32_16x16x32_f16 v[86:89], v[74:77], v[156:159], v[94:97]
	v_mfma_f32_16x16x32_f16 v[94:97], v[74:77], v[160:163], v[176:179]
	v_mfma_f32_16x16x32_f16 v[70:73], v[74:77], v[228:231], v[70:73]
	s_waitcnt vmcnt(18)
	v_mfma_f32_16x16x32_f16 v[54:57], v[66:69], v[38:41], v[54:57]
	v_mfma_f32_16x16x32_f16 v[74:77], v[66:69], v[156:159], v[90:93]
	v_mfma_f32_16x16x32_f16 v[90:93], v[66:69], v[160:163], v[180:183]
	v_mfma_f32_16x16x32_f16 v[62:65], v[66:69], v[228:231], v[62:65]
	s_waitcnt vmcnt(17)
	v_mfma_f32_16x16x32_f16 v[38:41], v[46:49], v[38:41], v[50:53]
	v_mfma_f32_16x16x32_f16 v[50:53], v[46:49], v[156:159], v[78:81]
	v_mfma_f32_16x16x32_f16 v[66:69], v[46:49], v[160:163], v[122:125]
	s_nop 1
	buffer_load_dwordx4 v[78:81], v147, s[16:19], s8 offen
	buffer_load_dwordx4 v[122:125], v148, s[16:19], s8 offen
	buffer_load_dwordx4 v[156:159], v149, s[16:19], s8 offen
	buffer_load_dwordx4 v[160:163], v150, s[16:19], s8 offen
	v_mfma_f32_16x16x32_f16 v[34:37], v[46:49], v[228:231], v[34:37]
	v_add_u32_e32 v98, s69, v98
	ds_read_b128 v[46:49], v98
	ds_read_b128 v[176:179], v98 offset:16384
	ds_read_b128 v[180:183], v98 offset:32768
	ds_read_b128 v[228:231], v98 offset:49152
	s_add_i32 s8, s22, s38
	s_waitcnt vmcnt(20) lgkmcnt(7)
	v_mfma_f32_16x16x32_f16 v[164:167], v[192:195], v[42:45], v[164:167]
	s_waitcnt lgkmcnt(6)
	v_mfma_f32_16x16x32_f16 v[168:171], v[192:195], v[208:211], v[168:171]
	s_waitcnt lgkmcnt(5)
	v_mfma_f32_16x16x32_f16 v[172:175], v[192:195], v[212:215], v[172:175]
	s_waitcnt lgkmcnt(4)
	v_mfma_f32_16x16x32_f16 v[82:85], v[192:195], v[216:219], v[82:85]
	s_waitcnt vmcnt(19)
	v_mfma_f32_16x16x32_f16 v[58:61], v[196:199], v[42:45], v[58:61]
	v_mfma_f32_16x16x32_f16 v[86:89], v[196:199], v[208:211], v[86:89]
	v_mfma_f32_16x16x32_f16 v[94:97], v[196:199], v[212:215], v[94:97]
	v_mfma_f32_16x16x32_f16 v[70:73], v[196:199], v[216:219], v[70:73]
	s_waitcnt vmcnt(18)
	v_mfma_f32_16x16x32_f16 v[54:57], v[200:203], v[42:45], v[54:57]
	v_mfma_f32_16x16x32_f16 v[74:77], v[200:203], v[208:211], v[74:77]
	v_mfma_f32_16x16x32_f16 v[90:93], v[200:203], v[212:215], v[90:93]
	v_mfma_f32_16x16x32_f16 v[62:65], v[200:203], v[216:219], v[62:65]
	s_waitcnt vmcnt(17)
	v_mfma_f32_16x16x32_f16 v[38:41], v[204:207], v[42:45], v[38:41]
	v_mfma_f32_16x16x32_f16 v[42:45], v[204:207], v[208:211], v[50:53]
	v_mfma_f32_16x16x32_f16 v[50:53], v[204:207], v[212:215], v[66:69]
	s_nop 2
	buffer_load_dwordx4 v[66:69], v147, s[16:19], s8 offen
	buffer_load_dwordx4 v[192:195], v148, s[16:19], s8 offen
	buffer_load_dwordx4 v[196:199], v149, s[16:19], s8 offen
	buffer_load_dwordx4 v[200:203], v150, s[16:19], s8 offen
	v_mfma_f32_16x16x32_f16 v[34:37], v[204:207], v[216:219], v[34:37]
	v_add_u32_e32 v99, s70, v99
	ds_read_b128 v[204:207], v99
	ds_read_b128 v[208:211], v99 offset:16384
	ds_read_b128 v[212:215], v99 offset:32768
	ds_read_b128 v[216:219], v99 offset:49152
	s_add_i32 s8, s22, s39
	s_waitcnt vmcnt(20) lgkmcnt(7)
	v_mfma_f32_16x16x32_f16 v[164:167], v[140:143], v[46:49], v[164:167]
	s_waitcnt lgkmcnt(6)
	v_mfma_f32_16x16x32_f16 v[168:171], v[140:143], v[176:179], v[168:171]
	s_waitcnt lgkmcnt(5)
	v_mfma_f32_16x16x32_f16 v[172:175], v[140:143], v[180:183], v[172:175]
	s_waitcnt lgkmcnt(4)
	v_mfma_f32_16x16x32_f16 v[82:85], v[140:143], v[228:231], v[82:85]
	s_waitcnt vmcnt(19)
	v_mfma_f32_16x16x32_f16 v[58:61], v[220:223], v[46:49], v[58:61]
	v_mfma_f32_16x16x32_f16 v[86:89], v[220:223], v[176:179], v[86:89]
	s_waitcnt vmcnt(18)
	v_mfma_f32_16x16x32_f16 v[54:57], v[152:155], v[46:49], v[54:57]
	v_mfma_f32_16x16x32_f16 v[74:77], v[152:155], v[176:179], v[74:77]
	v_mfma_f32_16x16x32_f16 v[90:93], v[152:155], v[180:183], v[90:93]
	v_mfma_f32_16x16x32_f16 v[62:65], v[152:155], v[228:231], v[62:65]
	s_waitcnt vmcnt(17)
	v_mfma_f32_16x16x32_f16 v[38:41], v[224:227], v[46:49], v[38:41]
	v_mfma_f32_16x16x32_f16 v[42:45], v[224:227], v[176:179], v[42:45]
	v_mfma_f32_16x16x32_f16 v[46:49], v[224:227], v[180:183], v[50:53]
	s_nop 2
	buffer_load_dwordx4 v[50:53], v147, s[16:19], s8 offen
	buffer_load_dwordx4 v[140:143], v148, s[16:19], s8 offen
	buffer_load_dwordx4 v[152:155], v149, s[16:19], s8 offen
	buffer_load_dwordx4 v[176:179], v150, s[16:19], s8 offen
	v_mfma_f32_16x16x32_f16 v[94:97], v[220:223], v[180:183], v[94:97]
	v_mfma_f32_16x16x32_f16 v[70:73], v[220:223], v[228:231], v[70:73]
	v_mfma_f32_16x16x32_f16 v[34:37], v[224:227], v[228:231], v[34:37]
	v_add_u32_e32 v100, s71, v100
	ds_read_b128 v[180:183], v100
	ds_read_b128 v[220:223], v100 offset:16384
	ds_read_b128 v[224:227], v100 offset:32768
	ds_read_b128 v[228:231], v100 offset:49152
	s_add_i32 s8, s22, s40
	s_waitcnt vmcnt(15) lgkmcnt(7)
	v_mfma_f32_16x16x32_f16 v[164:167], v[126:129], v[204:207], v[164:167]
	s_waitcnt lgkmcnt(6)
	v_mfma_f32_16x16x32_f16 v[168:171], v[126:129], v[208:211], v[168:171]
	s_waitcnt lgkmcnt(5)
	v_mfma_f32_16x16x32_f16 v[172:175], v[126:129], v[212:215], v[172:175]
	s_waitcnt lgkmcnt(4)
	v_mfma_f32_16x16x32_f16 v[82:85], v[126:129], v[216:219], v[82:85]
	s_waitcnt vmcnt(14)
	v_mfma_f32_16x16x32_f16 v[58:61], v[136:139], v[204:207], v[58:61]
	v_mfma_f32_16x16x32_f16 v[86:89], v[136:139], v[208:211], v[86:89]
	v_mfma_f32_16x16x32_f16 v[94:97], v[136:139], v[212:215], v[94:97]
	v_mfma_f32_16x16x32_f16 v[70:73], v[136:139], v[216:219], v[70:73]
	s_waitcnt vmcnt(13)
	v_mfma_f32_16x16x32_f16 v[54:57], v[184:187], v[204:207], v[54:57]
	v_mfma_f32_16x16x32_f16 v[74:77], v[184:187], v[208:211], v[74:77]
	v_mfma_f32_16x16x32_f16 v[90:93], v[184:187], v[212:215], v[90:93]
	v_mfma_f32_16x16x32_f16 v[62:65], v[184:187], v[216:219], v[62:65]
	s_waitcnt vmcnt(12)
	v_mfma_f32_16x16x32_f16 v[38:41], v[188:191], v[204:207], v[38:41]
	buffer_load_dwordx4 v[126:129], v147, s[16:19], s8 offen
	buffer_load_dwordx4 v[136:139], v148, s[16:19], s8 offen
	buffer_load_dwordx4 v[184:187], v149, s[16:19], s8 offen
	buffer_load_dwordx4 v[204:207], v150, s[16:19], s8 offen
	v_mfma_f32_16x16x32_f16 v[42:45], v[188:191], v[208:211], v[42:45]
	v_mfma_f32_16x16x32_f16 v[46:49], v[188:191], v[212:215], v[46:49]
	v_mfma_f32_16x16x32_f16 v[34:37], v[188:191], v[216:219], v[34:37]
	v_add_u32_e32 v111, s72, v111
	ds_read_b128 v[188:191], v111
	ds_read_b128 v[208:211], v111 offset:16384
	ds_read_b128 v[212:215], v111 offset:32768
	ds_read_b128 v[216:219], v111 offset:49152
	s_add_i32 s8, s22, s41
	s_waitcnt vmcnt(15) lgkmcnt(7)
	v_mfma_f32_16x16x32_f16 v[164:167], v[78:81], v[180:183], v[164:167]
	s_waitcnt lgkmcnt(6)
	v_mfma_f32_16x16x32_f16 v[168:171], v[78:81], v[220:223], v[168:171]
	s_waitcnt lgkmcnt(5)
	v_mfma_f32_16x16x32_f16 v[172:175], v[78:81], v[224:227], v[172:175]
	s_waitcnt lgkmcnt(4)
	v_mfma_f32_16x16x32_f16 v[78:81], v[78:81], v[228:231], v[82:85]
	s_waitcnt vmcnt(14)
	v_mfma_f32_16x16x32_f16 v[58:61], v[122:125], v[180:183], v[58:61]
	v_mfma_f32_16x16x32_f16 v[82:85], v[122:125], v[220:223], v[86:89]
	v_mfma_f32_16x16x32_f16 v[86:89], v[122:125], v[224:227], v[94:97]
	v_mfma_f32_16x16x32_f16 v[70:73], v[122:125], v[228:231], v[70:73]
	s_waitcnt vmcnt(13)
	v_mfma_f32_16x16x32_f16 v[54:57], v[156:159], v[180:183], v[54:57]
	v_mfma_f32_16x16x32_f16 v[74:77], v[156:159], v[220:223], v[74:77]
	v_mfma_f32_16x16x32_f16 v[90:93], v[156:159], v[224:227], v[90:93]
	v_mfma_f32_16x16x32_f16 v[62:65], v[156:159], v[228:231], v[62:65]
	s_waitcnt vmcnt(12)
	v_mfma_f32_16x16x32_f16 v[38:41], v[160:163], v[180:183], v[38:41]
	buffer_load_dwordx4 v[94:97], v147, s[16:19], s8 offen
	buffer_load_dwordx4 v[122:125], v148, s[16:19], s8 offen
	buffer_load_dwordx4 v[156:159], v149, s[16:19], s8 offen
	buffer_load_dwordx4 v[180:183], v150, s[16:19], s8 offen
	v_mfma_f32_16x16x32_f16 v[42:45], v[160:163], v[220:223], v[42:45]
	v_mfma_f32_16x16x32_f16 v[46:49], v[160:163], v[224:227], v[46:49]
	v_mfma_f32_16x16x32_f16 v[34:37], v[160:163], v[228:231], v[34:37]
	v_add_u32_e32 v98, s73, v98
	ds_read_b128 v[160:163], v98
	ds_read_b128 v[220:223], v98 offset:16384
	ds_read_b128 v[224:227], v98 offset:32768
	ds_read_b128 v[228:231], v98 offset:49152
	s_add_i32 s8, s22, s42
	s_waitcnt vmcnt(15) lgkmcnt(7)
	v_mfma_f32_16x16x32_f16 v[164:167], v[66:69], v[188:191], v[164:167]
	s_waitcnt lgkmcnt(6)
	v_mfma_f32_16x16x32_f16 v[168:171], v[66:69], v[208:211], v[168:171]
	s_waitcnt lgkmcnt(5)
	v_mfma_f32_16x16x32_f16 v[172:175], v[66:69], v[212:215], v[172:175]
	s_waitcnt lgkmcnt(4)
	v_mfma_f32_16x16x32_f16 v[66:69], v[66:69], v[216:219], v[78:81]
	s_waitcnt vmcnt(14)
	v_mfma_f32_16x16x32_f16 v[58:61], v[192:195], v[188:191], v[58:61]
	v_mfma_f32_16x16x32_f16 v[78:81], v[192:195], v[208:211], v[82:85]
	v_mfma_f32_16x16x32_f16 v[82:85], v[192:195], v[212:215], v[86:89]
	v_mfma_f32_16x16x32_f16 v[70:73], v[192:195], v[216:219], v[70:73]
	s_waitcnt vmcnt(13)
	v_mfma_f32_16x16x32_f16 v[54:57], v[196:199], v[188:191], v[54:57]
	v_mfma_f32_16x16x32_f16 v[74:77], v[196:199], v[208:211], v[74:77]
	v_mfma_f32_16x16x32_f16 v[86:89], v[196:199], v[212:215], v[90:93]
	v_mfma_f32_16x16x32_f16 v[62:65], v[196:199], v[216:219], v[62:65]
	s_waitcnt vmcnt(12)
	v_mfma_f32_16x16x32_f16 v[38:41], v[200:203], v[188:191], v[38:41]
	buffer_load_dwordx4 v[90:93], v147, s[16:19], s8 offen
	buffer_load_dwordx4 v[188:191], v148, s[16:19], s8 offen
	buffer_load_dwordx4 v[192:195], v149, s[16:19], s8 offen
	buffer_load_dwordx4 v[196:199], v150, s[16:19], s8 offen
	v_mfma_f32_16x16x32_f16 v[42:45], v[200:203], v[208:211], v[42:45]
	v_mfma_f32_16x16x32_f16 v[46:49], v[200:203], v[212:215], v[46:49]
	v_mfma_f32_16x16x32_f16 v[34:37], v[200:203], v[216:219], v[34:37]
	v_add_u32_e32 v99, s74, v99
	ds_read_b128 v[200:203], v99
	ds_read_b128 v[208:211], v99 offset:16384
	ds_read_b128 v[212:215], v99 offset:32768
	ds_read_b128 v[216:219], v99 offset:49152
	s_add_i32 s8, s22, s43
	s_waitcnt vmcnt(15) lgkmcnt(7)
	v_mfma_f32_16x16x32_f16 v[164:167], v[50:53], v[160:163], v[164:167]
	s_waitcnt lgkmcnt(6)
	v_mfma_f32_16x16x32_f16 v[168:171], v[50:53], v[220:223], v[168:171]
	s_waitcnt lgkmcnt(5)
	v_mfma_f32_16x16x32_f16 v[172:175], v[50:53], v[224:227], v[172:175]
	s_waitcnt lgkmcnt(4)
	v_mfma_f32_16x16x32_f16 v[50:53], v[50:53], v[228:231], v[66:69]
	s_waitcnt vmcnt(14)
	v_mfma_f32_16x16x32_f16 v[58:61], v[140:143], v[160:163], v[58:61]
	v_mfma_f32_16x16x32_f16 v[66:69], v[140:143], v[220:223], v[78:81]
	v_mfma_f32_16x16x32_f16 v[78:81], v[140:143], v[224:227], v[82:85]
	v_mfma_f32_16x16x32_f16 v[70:73], v[140:143], v[228:231], v[70:73]
	s_waitcnt vmcnt(13)
	v_mfma_f32_16x16x32_f16 v[54:57], v[152:155], v[160:163], v[54:57]
	v_mfma_f32_16x16x32_f16 v[74:77], v[152:155], v[220:223], v[74:77]
	v_mfma_f32_16x16x32_f16 v[82:85], v[152:155], v[224:227], v[86:89]
	v_mfma_f32_16x16x32_f16 v[62:65], v[152:155], v[228:231], v[62:65]
	s_waitcnt vmcnt(12)
	v_mfma_f32_16x16x32_f16 v[38:41], v[176:179], v[160:163], v[38:41]
	buffer_load_dwordx4 v[86:89], v147, s[16:19], s8 offen
	buffer_load_dwordx4 v[140:143], v148, s[16:19], s8 offen
	buffer_load_dwordx4 v[152:155], v149, s[16:19], s8 offen
	buffer_load_dwordx4 v[160:163], v150, s[16:19], s8 offen
	v_mfma_f32_16x16x32_f16 v[42:45], v[176:179], v[220:223], v[42:45]
	v_mfma_f32_16x16x32_f16 v[46:49], v[176:179], v[224:227], v[46:49]
	v_mfma_f32_16x16x32_f16 v[34:37], v[176:179], v[228:231], v[34:37]
	v_add_u32_e32 v100, s75, v100
	ds_read_b128 v[176:179], v100
	ds_read_b128 v[220:223], v100 offset:16384
	ds_read_b128 v[224:227], v100 offset:32768
	ds_read_b128 v[228:231], v100 offset:49152
	s_add_i32 s8, s22, s44
	s_waitcnt vmcnt(15) lgkmcnt(7)
	v_mfma_f32_16x16x32_f16 v[164:167], v[126:129], v[200:203], v[164:167]
	s_waitcnt lgkmcnt(6)
	v_mfma_f32_16x16x32_f16 v[168:171], v[126:129], v[208:211], v[168:171]
	s_waitcnt lgkmcnt(5)
	v_mfma_f32_16x16x32_f16 v[172:175], v[126:129], v[212:215], v[172:175]
	s_waitcnt lgkmcnt(4)
	v_mfma_f32_16x16x32_f16 v[50:53], v[126:129], v[216:219], v[50:53]
	s_waitcnt vmcnt(14)
	v_mfma_f32_16x16x32_f16 v[58:61], v[136:139], v[200:203], v[58:61]
	v_mfma_f32_16x16x32_f16 v[66:69], v[136:139], v[208:211], v[66:69]
	v_mfma_f32_16x16x32_f16 v[78:81], v[136:139], v[212:215], v[78:81]
	v_mfma_f32_16x16x32_f16 v[70:73], v[136:139], v[216:219], v[70:73]
	s_waitcnt vmcnt(13)
	v_mfma_f32_16x16x32_f16 v[54:57], v[184:187], v[200:203], v[54:57]
	v_mfma_f32_16x16x32_f16 v[74:77], v[184:187], v[208:211], v[74:77]
	v_mfma_f32_16x16x32_f16 v[82:85], v[184:187], v[212:215], v[82:85]
	v_mfma_f32_16x16x32_f16 v[62:65], v[184:187], v[216:219], v[62:65]
	s_waitcnt vmcnt(12)
	v_mfma_f32_16x16x32_f16 v[38:41], v[204:207], v[200:203], v[38:41]
	buffer_load_dwordx4 v[126:129], v147, s[16:19], s8 offen
	buffer_load_dwordx4 v[136:139], v148, s[16:19], s8 offen
	buffer_load_dwordx4 v[184:187], v149, s[16:19], s8 offen
	buffer_load_dwordx4 v[200:203], v150, s[16:19], s8 offen
	v_mfma_f32_16x16x32_f16 v[42:45], v[204:207], v[208:211], v[42:45]
	v_mfma_f32_16x16x32_f16 v[46:49], v[204:207], v[212:215], v[46:49]
	v_mfma_f32_16x16x32_f16 v[34:37], v[204:207], v[216:219], v[34:37]
	v_add_u32_e32 v111, s76, v111
	ds_read_b128 v[204:207], v111
	ds_read_b128 v[208:211], v111 offset:16384
	ds_read_b128 v[212:215], v111 offset:32768
	ds_read_b128 v[216:219], v111 offset:49152
	s_add_i32 s8, s22, s45
	s_waitcnt vmcnt(15) lgkmcnt(7)
	v_mfma_f32_16x16x32_f16 v[164:167], v[94:97], v[176:179], v[164:167]
	s_waitcnt lgkmcnt(6)
	v_mfma_f32_16x16x32_f16 v[168:171], v[94:97], v[220:223], v[168:171]
	s_waitcnt vmcnt(14)
	v_mfma_f32_16x16x32_f16 v[58:61], v[122:125], v[176:179], v[58:61]
	v_mfma_f32_16x16x32_f16 v[66:69], v[122:125], v[220:223], v[66:69]
	s_waitcnt lgkmcnt(5)
	v_mfma_f32_16x16x32_f16 v[78:81], v[122:125], v[224:227], v[78:81]
	s_waitcnt lgkmcnt(4)
	v_mfma_f32_16x16x32_f16 v[70:73], v[122:125], v[228:231], v[70:73]
	s_waitcnt vmcnt(13)
	v_mfma_f32_16x16x32_f16 v[54:57], v[156:159], v[176:179], v[54:57]
	v_mfma_f32_16x16x32_f16 v[74:77], v[156:159], v[220:223], v[74:77]
	v_mfma_f32_16x16x32_f16 v[82:85], v[156:159], v[224:227], v[82:85]
	v_mfma_f32_16x16x32_f16 v[62:65], v[156:159], v[228:231], v[62:65]
	s_waitcnt vmcnt(12)
	v_mfma_f32_16x16x32_f16 v[38:41], v[180:183], v[176:179], v[38:41]
	v_mfma_f32_16x16x32_f16 v[42:45], v[180:183], v[220:223], v[42:45]
	buffer_load_dwordx4 v[122:125], v147, s[16:19], s8 offen
	buffer_load_dwordx4 v[156:159], v148, s[16:19], s8 offen
	buffer_load_dwordx4 v[176:179], v149, s[16:19], s8 offen
	buffer_load_dwordx4 v[220:223], v150, s[16:19], s8 offen
	v_mfma_f32_16x16x32_f16 v[50:53], v[94:97], v[228:231], v[50:53]
	v_mfma_f32_16x16x32_f16 v[46:49], v[180:183], v[224:227], v[46:49]
	v_mfma_f32_16x16x32_f16 v[34:37], v[180:183], v[228:231], v[34:37]
	v_mfma_f32_16x16x32_f16 v[172:175], v[94:97], v[224:227], v[172:175]
	v_add_u32_e32 v98, s77, v98
	ds_read_b128 v[94:97], v98
	ds_read_b128 v[180:183], v98 offset:16384
	ds_read_b128 v[224:227], v98 offset:32768
	ds_read_b128 v[228:231], v98 offset:49152
	s_add_i32 s8, s22, s46
	s_waitcnt vmcnt(15) lgkmcnt(7)
	v_mfma_f32_16x16x32_f16 v[164:167], v[90:93], v[204:207], v[164:167]
	s_waitcnt lgkmcnt(6)
	v_mfma_f32_16x16x32_f16 v[168:171], v[90:93], v[208:211], v[168:171]
	s_waitcnt lgkmcnt(5)
	v_mfma_f32_16x16x32_f16 v[172:175], v[90:93], v[212:215], v[172:175]
	s_waitcnt lgkmcnt(4)
	v_mfma_f32_16x16x32_f16 v[90:93], v[90:93], v[216:219], v[50:53]
	s_waitcnt vmcnt(14)
	v_mfma_f32_16x16x32_f16 v[232:235], v[188:191], v[204:207], v[58:61]
	v_mfma_f32_16x16x32_f16 v[66:69], v[188:191], v[208:211], v[66:69]
	v_mfma_f32_16x16x32_f16 v[78:81], v[188:191], v[212:215], v[78:81]
	v_mfma_f32_16x16x32_f16 v[70:73], v[188:191], v[216:219], v[70:73]
	s_waitcnt vmcnt(13)
	v_mfma_f32_16x16x32_f16 v[188:191], v[192:195], v[204:207], v[54:57]
	v_mfma_f32_16x16x32_f16 v[74:77], v[192:195], v[208:211], v[74:77]
	v_mfma_f32_16x16x32_f16 v[82:85], v[192:195], v[212:215], v[82:85]
	v_mfma_f32_16x16x32_f16 v[62:65], v[192:195], v[216:219], v[62:65]
	s_waitcnt vmcnt(12)
	v_mfma_f32_16x16x32_f16 v[192:195], v[196:199], v[204:207], v[38:41]
	buffer_load_dwordx4 v[58:61], v147, s[16:19], s8 offen
	buffer_load_dwordx4 v[54:57], v148, s[16:19], s8 offen
	buffer_load_dwordx4 v[50:53], v149, s[16:19], s8 offen
	buffer_load_dwordx4 v[38:41], v150, s[16:19], s8 offen
	v_mfma_f32_16x16x32_f16 v[42:45], v[196:199], v[208:211], v[42:45]
	v_mfma_f32_16x16x32_f16 v[46:49], v[196:199], v[212:215], v[46:49]
	v_mfma_f32_16x16x32_f16 v[196:199], v[196:199], v[216:219], v[34:37]
	v_add_u32_e32 v99, s78, v99
	ds_read_b128 v[204:207], v99
	ds_read_b128 v[208:211], v99 offset:16384
	ds_read_b128 v[212:215], v99 offset:32768
	ds_read_b128 v[216:219], v99 offset:49152
	s_add_i32 s8, s22, s47
	s_waitcnt vmcnt(15) lgkmcnt(7)
	v_mfma_f32_16x16x32_f16 v[164:167], v[86:89], v[94:97], v[164:167]
	s_waitcnt lgkmcnt(6)
	v_mfma_f32_16x16x32_f16 v[168:171], v[86:89], v[180:183], v[168:171]
	s_waitcnt lgkmcnt(5)
	v_mfma_f32_16x16x32_f16 v[172:175], v[86:89], v[224:227], v[172:175]
	s_waitcnt lgkmcnt(4)
	v_mfma_f32_16x16x32_f16 v[86:89], v[86:89], v[228:231], v[90:93]
	s_waitcnt vmcnt(14)
	v_mfma_f32_16x16x32_f16 v[232:235], v[140:143], v[94:97], v[232:235]
	v_mfma_f32_16x16x32_f16 v[66:69], v[140:143], v[180:183], v[66:69]
	v_mfma_f32_16x16x32_f16 v[236:239], v[140:143], v[224:227], v[78:81]
	v_mfma_f32_16x16x32_f16 v[70:73], v[140:143], v[228:231], v[70:73]
	s_waitcnt vmcnt(13)
	v_mfma_f32_16x16x32_f16 v[140:143], v[152:155], v[94:97], v[188:191]
	v_mfma_f32_16x16x32_f16 v[74:77], v[152:155], v[180:183], v[74:77]
	v_mfma_f32_16x16x32_f16 v[82:85], v[152:155], v[224:227], v[82:85]
	v_mfma_f32_16x16x32_f16 v[62:65], v[152:155], v[228:231], v[62:65]
	s_waitcnt vmcnt(12)
	v_mfma_f32_16x16x32_f16 v[152:155], v[160:163], v[94:97], v[192:195]
	buffer_load_dwordx4 v[94:97], v147, s[16:19], s8 offen
	buffer_load_dwordx4 v[90:93], v148, s[16:19], s8 offen
	buffer_load_dwordx4 v[78:81], v149, s[16:19], s8 offen
	buffer_load_dwordx4 v[34:37], v150, s[16:19], s8 offen
	v_mfma_f32_16x16x32_f16 v[42:45], v[160:163], v[180:183], v[42:45]
	v_mfma_f32_16x16x32_f16 v[46:49], v[160:163], v[224:227], v[46:49]
	v_mfma_f32_16x16x32_f16 v[160:163], v[160:163], v[228:231], v[196:199]
	v_add_u32_e32 v100, s79, v100
	ds_read_b128 v[180:183], v100
	ds_read_b128 v[188:191], v100 offset:16384
	ds_read_b128 v[192:195], v100 offset:32768
	ds_read_b128 v[196:199], v100 offset:49152
	s_add_i32 s8, s22, s48
	s_waitcnt vmcnt(15) lgkmcnt(7)
	v_mfma_f32_16x16x32_f16 v[164:167], v[126:129], v[204:207], v[164:167]
	s_waitcnt lgkmcnt(6)
	v_mfma_f32_16x16x32_f16 v[168:171], v[126:129], v[208:211], v[168:171]
	s_waitcnt lgkmcnt(5)
	v_mfma_f32_16x16x32_f16 v[172:175], v[126:129], v[212:215], v[172:175]
	s_waitcnt lgkmcnt(4)
	v_mfma_f32_16x16x32_f16 v[86:89], v[126:129], v[216:219], v[86:89]
	s_waitcnt vmcnt(14)
	v_mfma_f32_16x16x32_f16 v[126:129], v[136:139], v[204:207], v[232:235]
	v_mfma_f32_16x16x32_f16 v[66:69], v[136:139], v[208:211], v[66:69]
	v_mfma_f32_16x16x32_f16 v[224:227], v[136:139], v[212:215], v[236:239]
	v_mfma_f32_16x16x32_f16 v[136:139], v[136:139], v[216:219], v[70:73]
	s_waitcnt vmcnt(13)
	v_mfma_f32_16x16x32_f16 v[140:143], v[184:187], v[204:207], v[140:143]
	v_mfma_f32_16x16x32_f16 v[74:77], v[184:187], v[208:211], v[74:77]
	v_mfma_f32_16x16x32_f16 v[228:231], v[184:187], v[212:215], v[82:85]
	v_mfma_f32_16x16x32_f16 v[184:187], v[184:187], v[216:219], v[62:65]
	s_waitcnt vmcnt(12)
	v_mfma_f32_16x16x32_f16 v[152:155], v[200:203], v[204:207], v[152:155]
	v_mfma_f32_16x16x32_f16 v[204:207], v[200:203], v[208:211], v[42:45]
	buffer_load_dwordx4 v[82:85], v147, s[16:19], s8 offen
	buffer_load_dwordx4 v[70:73], v148, s[16:19], s8 offen
	buffer_load_dwordx4 v[62:65], v149, s[16:19], s8 offen
	buffer_load_dwordx4 v[42:45], v150, s[16:19], s8 offen
	v_mfma_f32_16x16x32_f16 v[46:49], v[200:203], v[212:215], v[46:49]
	v_mfma_f32_16x16x32_f16 v[160:163], v[200:203], v[216:219], v[160:163]
	v_add_u32_e32 v0, 0x1ac00, v104
	ds_read_b128 v[240:243], v0
	ds_read_b128 v[244:247], v0 offset:16
	s_waitcnt vmcnt(12) lgkmcnt(5)
	v_mfma_f32_16x16x32_f16 v[164:167], v[122:125], v[180:183], v[164:167]
	v_mfma_f32_16x16x32_f16 v[126:129], v[156:159], v[180:183], v[126:129]
	v_mfma_f32_16x16x32_f16 v[140:143], v[176:179], v[180:183], v[140:143]
	v_mfma_f32_16x16x32_f16 v[152:155], v[220:223], v[180:183], v[152:155]
	s_waitcnt lgkmcnt(4)
	v_mfma_f32_16x16x32_f16 v[168:171], v[122:125], v[188:191], v[168:171]
	v_mfma_f32_16x16x32_f16 v[208:211], v[156:159], v[188:191], v[66:69]
	v_mfma_f32_16x16x32_f16 v[212:215], v[176:179], v[188:191], v[74:77]
	v_mfma_f32_16x16x32_f16 v[204:207], v[220:223], v[188:191], v[204:207]
	s_waitcnt lgkmcnt(3)
	v_mfma_f32_16x16x32_f16 v[172:175], v[122:125], v[192:195], v[172:175]
	v_cvt_pk_f16_f32 v232, v164, v165
	v_cvt_pk_f16_f32 v233, v166, v167
	v_pk_max_f16 v232, v232, 0
	v_pk_max_f16 v233, v233, 0
	v_mfma_f32_16x16x32_f16 v[224:227], v[156:159], v[192:195], v[224:227]
	v_cvt_pk_f16_f32 v234, v126, v127
	v_cvt_pk_f16_f32 v235, v128, v129
	v_pk_max_f16 v234, v234, 0
	v_pk_max_f16 v235, v235, 0
	v_mfma_f32_16x16x32_f16 v[228:231], v[176:179], v[192:195], v[228:231]
	v_cvt_pk_f16_f32 v236, v140, v141
	v_cvt_pk_f16_f32 v237, v142, v143
	v_pk_max_f16 v236, v236, 0
	v_pk_max_f16 v237, v237, 0
	v_mfma_f32_16x16x32_f16 v[216:219], v[220:223], v[192:195], v[46:49]
	v_cvt_pk_f16_f32 v238, v152, v153
	v_cvt_pk_f16_f32 v239, v154, v155
	v_pk_max_f16 v238, v238, 0
	v_pk_max_f16 v239, v239, 0
	s_waitcnt lgkmcnt(2)
	v_mfma_f32_16x16x32_f16 v[200:203], v[122:125], v[196:199], v[86:89]
	v_cvt_pk_f16_f32 v180, v168, v169
	v_cvt_pk_f16_f32 v181, v170, v171
	v_pk_max_f16 v180, v180, 0
	v_pk_max_f16 v181, v181, 0
	s_add_i32 s8, s22, s49
	buffer_load_dwordx4 v[86:89], v147, s[16:19], s8 offen
	buffer_load_dwordx4 v[74:77], v148, s[16:19], s8 offen
	buffer_load_dwordx4 v[66:69], v149, s[16:19], s8 offen
	buffer_load_dwordx4 v[46:49], v150, s[16:19], s8 offen
	v_mfma_f32_16x16x32_f16 v[136:139], v[156:159], v[196:199], v[136:139]
	v_cvt_pk_f16_f32 v182, v208, v209
	v_cvt_pk_f16_f32 v183, v210, v211
	v_pk_max_f16 v182, v182, 0
	v_pk_max_f16 v183, v183, 0
	s_waitcnt lgkmcnt(1)
	v_mfma_f32_16x16x32_f16 v[252:255], v[240:243], v[232:235], 0
	v_cvt_pk_f16_f32 v232, v172, v173
	v_cvt_pk_f16_f32 v233, v174, v175
	v_pk_max_f16 v232, v232, 0
	v_pk_max_f16 v233, v233, 0
	v_mfma_f32_16x16x32_f16 v[184:187], v[176:179], v[196:199], v[184:187]
	v_cvt_pk_f16_f32 v188, v212, v213
	v_cvt_pk_f16_f32 v189, v214, v215
	v_pk_max_f16 v188, v188, 0
	v_pk_max_f16 v189, v189, 0
	s_waitcnt lgkmcnt(0)
	v_mfma_f32_16x16x32_f16 v[252:255], v[244:247], v[236:239], v[252:255]
	ds_read_u16 v102, v114
	ds_read_u16 v103, v114 offset:512
	ds_read_u16 v115, v114 offset:1024
	ds_read_u16 v116, v114 offset:1536
	v_cvt_pk_f16_f32 v234, v224, v225
	v_cvt_pk_f16_f32 v235, v226, v227
	v_pk_max_f16 v234, v234, 0
	v_pk_max_f16 v235, v235, 0
	v_mfma_f32_16x16x32_f16 v[160:163], v[220:223], v[196:199], v[160:163]
	v_cvt_pk_f16_f32 v190, v204, v205
	v_cvt_pk_f16_f32 v191, v206, v207
	v_pk_max_f16 v190, v190, 0
	v_pk_max_f16 v191, v191, 0
	v_mfma_f32_16x16x32_f16 v[192:195], v[240:243], v[180:183], 0
	v_cvt_pk_f16_f32 v236, v228, v229
	v_cvt_pk_f16_f32 v237, v230, v231
	v_pk_max_f16 v236, v236, 0
	v_pk_max_f16 v237, v237, 0
	v_mfma_f32_16x16x32_f16 v[192:195], v[244:247], v[188:191], v[192:195]
	v_cvt_pk_f16_f32 v238, v216, v217
	v_cvt_pk_f16_f32 v239, v218, v219
	v_pk_max_f16 v238, v238, 0
	v_pk_max_f16 v239, v239, 0
	v_cvt_pk_f16_f32 v180, v200, v201
	v_cvt_pk_f16_f32 v181, v202, v203
	v_pk_max_f16 v180, v180, 0
	v_pk_max_f16 v181, v181, 0
	v_mfma_f32_16x16x32_f16 v[196:199], v[240:243], v[232:235], 0
	v_cvt_pk_f16_f32 v182, v136, v137
	v_cvt_pk_f16_f32 v183, v138, v139
	v_pk_max_f16 v182, v182, 0
	v_pk_max_f16 v183, v183, 0
	v_mfma_f32_16x16x32_f16 v[196:199], v[244:247], v[236:239], v[196:199]
	v_cvt_pk_f16_f32 v188, v184, v185
	v_cvt_pk_f16_f32 v189, v186, v187
	v_mfma_f32_16x16x32_f16 v[122:125], v[240:243], v[180:183], 0
	v_pk_max_f16 v188, v188, 0
	v_pk_max_f16 v189, v189, 0
	v_cvt_pk_f16_f32 v190, v160, v161
	v_cvt_pk_f16_f32 v191, v162, v163
	v_pk_max_f16 v190, v190, 0
	v_pk_max_f16 v191, v191, 0
	s_nop 1
	v_mfma_f32_16x16x32_f16 v[122:125], v[244:247], v[188:191], v[122:125]
	v_add_u32_e32 v145, 0x12c00, v105
	v_cndmask_b32_e64 v0, v252, v192, s[2:3]
	v_cndmask_b32_e64 v0, v0, v196, s[0:1]
	s_waitcnt vmcnt(16)
	v_cndmask_b32_e64 v1, v30, v134, s[0:1]
	v_bfi_b32 v30, s10, v1, v30
	v_perm_b32 v1, v22, v134, s24
	v_cndmask_b32_e64 v22, v22, v1, s[0:1]
	v_cndmask_b32_e64 v0, v0, v122, s[26:27]
	ds_write_b32 v112, v0
	v_bfi_b32 v1, s10, v135, v18
	v_perm_b32 v121, v10, v135, s24
	v_cndmask_b32_e64 v18, v18, v1, s[0:1]
	v_cndmask_b32_e64 v10, v10, v121, s[0:1]
	s_add_i32 s22, s22, 0x80000
	s_add_i32 s11, s11, 1
	s_add_u32 s12, s12, 4
	s_addc_u32 s13, s13, 0
	v_add_u32_e32 v104, 0x400, v104
	v_add_u32_e32 v105, 0x800, v105
	v_add_u32_e32 v114, 2, v114
	s_cmp_eq_u32 s22, 0x898000
	s_waitcnt lgkmcnt(0)
	s_barrier
	ds_read_b128 v[232:235], v113
	ds_read_b128 v[236:239], v113 offset:1024
	ds_read_b128 v[240:243], v145 offset:2048
	ds_read_b128 v[244:247], v145 offset:2064
	ds_read_b128 v[248:251], v145 offset:2080
	ds_read_b128 v[252:255], v145 offset:2096
	s_waitcnt lgkmcnt(4)
	v_add_f32_e32 v0, v232, v233
	v_add_f32_e32 v1, v234, v235
	v_add_f32_e32 v121, v236, v237
	v_add_f32_e32 v144, v238, v239
	v_add_f32_e32 v0, v0, v1
	v_add_f32_e32 v121, v121, v144
	v_add_f32_e32 v0, v0, v121
	v_add_f32_e32 v0, s30, v0
	v_cvt_f16_f32_e32 v1, v0
	v_cvt_f16_f32_e32 v121, v0
	ds_write_b32 v106, v0
	v_add_u32_e32 v106, 4, v106
	v_permlane16_swap_b32_e32 v1, v121
	s_cbranch_scc0 .LBB1_4
